# EpiResidual (GEMM2 layers>0, GEMM4): second row-half's residual loads issued with the first half's into spare registers, counted waits (vmcnt 8) instead of full drains
# speedup vs baseline: 1.0318x; 1.0048x over previous
; __device__ __forceinline__ unsigned cvt_pk_bf16(float lo, float hi) { unsigned r; asm volatile("v_cvt_pk_bf16_f32 %0, %1, %2" : "=v"(r) : "v"(lo), "v"(hi)); return r; }
; __device__ __forceinline__ void st_wt16(void* p, u32x4 v) { asm volatile("global_store_dwordx4 %0, %1, off sc1\n\ts_nop 1" :: "v"(p), "v"(v) : "memory"); }
;     __device__ __forceinline__ void operator()(const f32x4 (&acc)[2][2][4][2], const Unit& u, int wr, int wc, int fr, int fq) const {
;         const int row0 = u.pm * BM + wr * 64 + fr, col0 = u.pn * BM + wc * 32 + 8 * fq;
; #pragma unroll
;         for (int ai = 0; ai < 2; ++ai) {
;             u32x4 bb[4][2]; f32x4 bf0[4][2], bf1[4][2];
; #pragma unroll
;             for (int m = 0; m < 4; ++m)
; #pragma unroll
;                 for (int bj = 0; bj < 2; ++bj) { const size_t off = (size_t)(row0 + ai * HALF + m * 16) * D + col0 + bj * HALF;
;                     if constexpr (BASE_F32) { bf0[m][bj] = *(const f32x4*)(basef + off); bf1[m][bj] = *(const f32x4*)(basef + off + 4); } else bb[m][bj] = *(const u32x4*)(hb + off); }
;             u32x2 p8[4][2];
; #pragma unroll
;             for (int m = 0; m < 4; ++m) {
;                 const int row = row0 + ai * HALF + m * 16; const size_t off = (size_t)row * D + col0; float ss = 0.f;
; #pragma unroll
;                 for (int bj = 0; bj < 2; ++bj) {
;                     f32x4 h0, h1;
;                     if constexpr (BASE_F32) { h0 = bf0[m][bj]; h1 = bf1[m][bj]; }
;                     else { const u32x4 b = bb[m][bj];
;                         h0 = (f32x4){__uint_as_float(b.x << 16), __uint_as_float(b.x & 0xffff0000u), __uint_as_float(b.y << 16), __uint_as_float(b.y & 0xffff0000u)};
;                         h1 = (f32x4){__uint_as_float(b.z << 16), __uint_as_float(b.z & 0xffff0000u), __uint_as_float(b.w << 16), __uint_as_float(b.w & 0xffff0000u)}; }
;                     h0 = h0 + acc[ai][bj][m][0]; h1 = h1 + acc[ai][bj][m][1];
;                     u32x4 w; w.x = cvt_pk_bf16(h0[0], h0[1]); w.y = cvt_pk_bf16(h0[2], h0[3]); w.z = cvt_pk_bf16(h1[0], h1[1]); w.w = cvt_pk_bf16(h1[2], h1[3]);
;                     if (WT && wt) st_wt16(hb + HO + off + bj * HALF, w); else *(u32x4*)(hb + HO + off + bj * HALF) = w;
.LBB0_756:
	v_mbcnt_lo_u32_b32 v130, -1, 0
	v_mbcnt_hi_u32_b32 v130, -1, v130
	s_lshl_b32 s4, s14, 8
	v_add_u32_e32 v130, s93, v130
	s_add_i32 s4, s4, s47
	v_and_b32_e32 v194, 15, v130
	v_or_b32_e32 v168, s4, v194
	s_lshl_b32 s4, s28, 8
	v_bfe_u32 v195, v130, 4, 2
	s_or_b32 s4, s4, s48
	v_lshl_or_b32 v166, v195, 3, s4
	v_ashrrev_i32_e32 v167, 31, v166
	v_lshlrev_b64 v[188:189], 1, v[166:167]
	v_ashrrev_i32_e32 v169, 31, v168
	v_or_b32_e32 v180, 16, v168
	v_lshl_add_u64 v[170:171], s[8:9], 0, v[188:189]
	v_lshlrev_b64 v[190:191], 11, v[168:169]
	v_ashrrev_i32_e32 v181, 31, v180
	v_or_b32_e32 v176, 32, v168
	v_lshl_add_u64 v[130:131], v[170:171], 0, v[190:191]
	v_lshlrev_b64 v[182:183], 11, v[180:181]
	v_ashrrev_i32_e32 v177, 31, v176
	v_or_b32_e32 v172, 48, v168
	global_load_dwordx4 v[184:187], v[130:131], off
	global_load_dwordx4 v[154:157], v[130:131], off offset:256
	v_lshl_add_u64 v[130:131], v[170:171], 0, v[182:183]
	v_lshlrev_b64 v[178:179], 11, v[176:177]
	v_ashrrev_i32_e32 v173, 31, v172
	global_load_dwordx4 v[150:153], v[130:131], off
	global_load_dwordx4 v[146:149], v[130:131], off offset:256
	v_lshl_add_u64 v[130:131], v[170:171], 0, v[178:179]
	v_lshlrev_b64 v[174:175], 11, v[172:173]
	global_load_dwordx4 v[142:145], v[130:131], off
	global_load_dwordx4 v[138:141], v[130:131], off offset:256
	v_lshl_add_u64 v[130:131], v[170:171], 0, v[174:175]
	global_load_dwordx4 v[134:137], v[130:131], off
	s_nop 0
	global_load_dwordx4 v[130:133], v[130:131], off offset:256
	s_mov_b64 s[100:101], 0x40000
	v_lshl_add_u64 v[216:217], v[170:171], 0, v[190:191]
	v_lshl_add_u64 v[216:217], v[216:217], 0, s[100:101]
	global_load_dwordx4 v[230:233], v[216:217], off
	global_load_dwordx4 v[234:237], v[216:217], off offset:256
	v_lshl_add_u64 v[216:217], v[170:171], 0, v[182:183]
	v_lshl_add_u64 v[216:217], v[216:217], 0, s[100:101]
	global_load_dwordx4 v[238:241], v[216:217], off
	global_load_dwordx4 v[242:245], v[216:217], off offset:256
	v_lshl_add_u64 v[216:217], v[170:171], 0, v[178:179]
	v_lshl_add_u64 v[216:217], v[216:217], 0, s[100:101]
	global_load_dwordx4 v[246:249], v[216:217], off
	global_load_dwordx4 v[250:253], v[216:217], off offset:256
	v_lshl_add_u64 v[216:217], v[170:171], 0, v[174:175]
	v_lshl_add_u64 v[216:217], v[216:217], 0, s[100:101]
	global_load_dwordx4 v[222:225], v[216:217], off
	global_load_dwordx4 v[212:215], v[216:217], off offset:256
	v_lshl_add_u64 v[190:191], s[8:9], 0, v[190:191]
	v_lshl_add_u64 v[190:191], v[190:191], 0, v[188:189]
	s_and_b64 vcc, exec, s[12:13]
	s_mov_b64 s[76:77], 0x100
	s_waitcnt vmcnt(8)
	v_lshlrev_b32_e32 v188, 16, v184
	v_and_b32_e32 v189, 0xffff0000, v184
	v_lshlrev_b32_e32 v184, 16, v185
	v_and_b32_e32 v185, 0xffff0000, v185
	v_lshlrev_b32_e32 v196, 16, v186
	v_and_b32_e32 v197, 0xffff0000, v186
	v_lshlrev_b32_e32 v186, 16, v187
	v_and_b32_e32 v187, 0xffff0000, v187
	v_pk_add_f32 v[184:185], v[128:129], v[184:185]
	v_pk_add_f32 v[188:189], v[126:127], v[188:189]
	v_pk_add_f32 v[126:127], v[124:125], v[186:187]
	v_pk_add_f32 v[128:129], v[122:123], v[196:197]
	v_cvt_pk_bf16_f32 v122, v188, v189
	v_cvt_pk_bf16_f32 v123, v184, v185
	s_nop 0
	v_cvt_pk_bf16_f32 v124, v128, v129
	v_cvt_pk_bf16_f32 v125, v126, v127
	s_cbranch_vccz .LBB0_842
	global_store_dwordx4 v[190:191], v[122:125], off
	s_cbranch_execnz .LBB0_759

; __device__ __forceinline__ unsigned cvt_pk_bf16(float lo, float hi) { unsigned r; asm volatile("v_cvt_pk_bf16_f32 %0, %1, %2" : "=v"(r) : "v"(lo), "v"(hi)); return r; }
; __device__ __forceinline__ void st_wt16(void* p, u32x4 v) { asm volatile("global_store_dwordx4 %0, %1, off sc1\n\ts_nop 1" :: "v"(p), "v"(v) : "memory"); }
;     __device__ __forceinline__ void operator()(const f32x4 (&acc)[2][2][4][2], const Unit& u, int wr, int wc, int fr, int fq) const {
;     ...
;         for (int ai = 0; ai < 2; ++ai) {
;             u32x4 bb[4][2]; f32x4 bf0[4][2], bf1[4][2];
; #pragma unroll
;             for (int m = 0; m < 4; ++m)
; #pragma unroll
;                 for (int bj = 0; bj < 2; ++bj) { const size_t off = (size_t)(row0 + ai * HALF + m * 16) * D + col0 + bj * HALF;
;                     if constexpr (BASE_F32) { bf0[m][bj] = *(const f32x4*)(basef + off); bf1[m][bj] = *(const f32x4*)(basef + off + 4); } else bb[m][bj] = *(const u32x4*)(hb + off); }
;             u32x2 p8[4][2];
; #pragma unroll
;             for (int m = 0; m < 4; ++m) {
;                 const int row = row0 + ai * HALF + m * 16; const size_t off = (size_t)row * D + col0; float ss = 0.f;
; #pragma unroll
;                 for (int bj = 0; bj < 2; ++bj) {
;                     f32x4 h0, h1;
;                     if constexpr (BASE_F32) { h0 = bf0[m][bj]; h1 = bf1[m][bj]; }
;                     else { const u32x4 b = bb[m][bj];
;                         h0 = (f32x4){__uint_as_float(b.x << 16), __uint_as_float(b.x & 0xffff0000u), __uint_as_float(b.y << 16), __uint_as_float(b.y & 0xffff0000u)};
;                         h1 = (f32x4){__uint_as_float(b.z << 16), __uint_as_float(b.z & 0xffff0000u), __uint_as_float(b.w << 16), __uint_as_float(b.w & 0xffff0000u)}; }
;                     h0 = h0 + acc[ai][bj][m][0]; h1 = h1 + acc[ai][bj][m][1];
;                     u32x4 w; w.x = cvt_pk_bf16(h0[0], h0[1]); w.y = cvt_pk_bf16(h0[2], h0[3]); w.z = cvt_pk_bf16(h1[0], h1[1]); w.w = cvt_pk_bf16(h1[2], h1[3]);
;                     if (WT && wt) st_wt16(hb + HO + off + bj * HALF, w); else *(u32x4*)(hb + HO + off + bj * HALF) = w;
.LBB0_796:
	s_or_b64 exec, exec, s[30:31]
	v_add_u32_e32 v106, 0x80, v168
	v_ashrrev_i32_e32 v107, 31, v106
	v_add_u32_e32 v102, 0x90, v168
	v_lshlrev_b64 v[112:113], 11, v[106:107]
	v_ashrrev_i32_e32 v103, 31, v102
	v_add_u32_e32 v98, 0xa0, v168
	v_lshl_add_u64 v[66:67], v[170:171], 0, v[112:113]
	v_lshlrev_b64 v[104:105], 11, v[102:103]
	v_ashrrev_i32_e32 v99, 31, v98
	v_add_u32_e32 v94, 0xb0, v168
	s_waitcnt vmcnt(8)
	v_mov_b64_e32 v[108:109], v[230:231]
	v_mov_b64_e32 v[110:111], v[232:233]
	v_mov_b64_e32 v[90:91], v[234:235]
	v_mov_b64_e32 v[92:93], v[236:237]
	v_lshl_add_u64 v[66:67], v[170:171], 0, v[104:105]
	v_lshlrev_b64 v[100:101], 11, v[98:99]
	v_ashrrev_i32_e32 v95, 31, v94
	v_mov_b64_e32 v[86:87], v[238:239]
	v_mov_b64_e32 v[88:89], v[240:241]
	v_mov_b64_e32 v[82:83], v[242:243]
	v_mov_b64_e32 v[84:85], v[244:245]
	v_lshl_add_u64 v[66:67], v[170:171], 0, v[100:101]
	v_lshlrev_b64 v[96:97], 11, v[94:95]
	v_mov_b64_e32 v[78:79], v[246:247]
	v_mov_b64_e32 v[80:81], v[248:249]
	v_mov_b64_e32 v[74:75], v[250:251]
	v_mov_b64_e32 v[76:77], v[252:253]
	v_lshl_add_u64 v[66:67], v[170:171], 0, v[96:97]
	v_mov_b64_e32 v[70:71], v[222:223]
	v_mov_b64_e32 v[72:73], v[224:225]
	s_nop 0
	v_mov_b64_e32 v[66:67], v[212:213]
	v_mov_b64_e32 v[68:69], v[214:215]
	v_lshl_add_u64 v[112:113], s[8:9], 0, v[112:113]
	s_and_b64 vcc, exec, s[4:5]
	v_lshl_add_u64 v[112:113], v[166:167], 1, v[112:113]
	v_lshlrev_b32_e32 v114, 16, v108
	v_and_b32_e32 v115, 0xffff0000, v108
	v_lshlrev_b32_e32 v108, 16, v109
	v_and_b32_e32 v109, 0xffff0000, v109
	v_lshlrev_b32_e32 v116, 16, v110
	v_and_b32_e32 v117, 0xffff0000, v110
	v_lshlrev_b32_e32 v118, 16, v111
	v_and_b32_e32 v119, 0xffff0000, v111
	v_pk_add_f32 v[108:109], v[62:63], v[108:109]
	v_pk_add_f32 v[110:111], v[60:61], v[114:115]
	v_pk_add_f32 v[60:61], v[58:59], v[118:119]
	v_pk_add_f32 v[62:63], v[56:57], v[116:117]
	v_cvt_pk_bf16_f32 v56, v110, v111
	v_cvt_pk_bf16_f32 v57, v108, v109
	s_nop 0
	v_cvt_pk_bf16_f32 v58, v62, v63
	v_cvt_pk_bf16_f32 v59, v60, v61
	s_cbranch_vccnz .LBB0_850
	global_store_dwordx4 v[112:113], v[56:59], off
	s_cbranch_execnz .LBB0_799

; __device__ __forceinline__ unsigned cvt_pk_bf16(float lo, float hi) { unsigned r; asm volatile("v_cvt_pk_bf16_f32 %0, %1, %2" : "=v"(r) : "v"(lo), "v"(hi)); return r; }
; __device__ __forceinline__ void st_wt16(void* p, u32x4 v) { asm volatile("global_store_dwordx4 %0, %1, off sc1\n\ts_nop 1" :: "v"(p), "v"(v) : "memory"); }
;     __device__ __forceinline__ void operator()(const f32x4 (&acc)[2][2][4][2], const Unit& u, int wr, int wc, int fr, int fq) const {
;         const int row0 = u.pm * BM + wr * 64 + fr, col0 = u.pn * BM + wc * 32 + 8 * fq;
; #pragma unroll
;         for (int ai = 0; ai < 2; ++ai) {
;             u32x4 bb[4][2]; f32x4 bf0[4][2], bf1[4][2];
; #pragma unroll
;             for (int m = 0; m < 4; ++m)
; #pragma unroll
;                 for (int bj = 0; bj < 2; ++bj) { const size_t off = (size_t)(row0 + ai * HALF + m * 16) * D + col0 + bj * HALF;
;                     if constexpr (BASE_F32) { bf0[m][bj] = *(const f32x4*)(basef + off); bf1[m][bj] = *(const f32x4*)(basef + off + 4); } else bb[m][bj] = *(const u32x4*)(hb + off); }
;             u32x2 p8[4][2];
; #pragma unroll
;             for (int m = 0; m < 4; ++m) {
;                 const int row = row0 + ai * HALF + m * 16; const size_t off = (size_t)row * D + col0; float ss = 0.f;
; #pragma unroll
;                 for (int bj = 0; bj < 2; ++bj) {
;                     f32x4 h0, h1;
;                     if constexpr (BASE_F32) { h0 = bf0[m][bj]; h1 = bf1[m][bj]; }
;                     else { const u32x4 b = bb[m][bj];
;                         h0 = (f32x4){__uint_as_float(b.x << 16), __uint_as_float(b.x & 0xffff0000u), __uint_as_float(b.y << 16), __uint_as_float(b.y & 0xffff0000u)};
;                         h1 = (f32x4){__uint_as_float(b.z << 16), __uint_as_float(b.z & 0xffff0000u), __uint_as_float(b.w << 16), __uint_as_float(b.w & 0xffff0000u)}; }
;                     h0 = h0 + acc[ai][bj][m][0]; h1 = h1 + acc[ai][bj][m][1];
;                     u32x4 w; w.x = cvt_pk_bf16(h0[0], h0[1]); w.y = cvt_pk_bf16(h0[2], h0[3]); w.z = cvt_pk_bf16(h1[0], h1[1]); w.w = cvt_pk_bf16(h1[2], h1[3]);
;                     if (WT && wt) st_wt16(hb + HO + off + bj * HALF, w); else *(u32x4*)(hb + HO + off + bj * HALF) = w;
.LBB0_1305:
	v_mbcnt_lo_u32_b32 v130, -1, 0
	v_mbcnt_hi_u32_b32 v130, -1, v130
	s_lshl_b32 s4, s8, 8
	v_add_u32_e32 v130, s93, v130
	s_add_i32 s4, s4, s65
	v_and_b32_e32 v190, 15, v130
	v_or_b32_e32 v164, s4, v190
	s_lshl_b32 s4, s28, 8
	v_bfe_u32 v191, v130, 4, 2
	s_or_b32 s4, s4, s68
	v_lshl_or_b32 v162, v191, 3, s4
	v_ashrrev_i32_e32 v163, 31, v162
	v_lshlrev_b64 v[184:185], 1, v[162:163]
	v_ashrrev_i32_e32 v165, 31, v164
	v_or_b32_e32 v176, 16, v164
	v_lshl_add_u64 v[166:167], s[12:13], 0, v[184:185]
	v_lshlrev_b64 v[186:187], 11, v[164:165]
	v_ashrrev_i32_e32 v177, 31, v176
	v_or_b32_e32 v172, 32, v164
	v_lshl_add_u64 v[130:131], v[166:167], 0, v[186:187]
	v_lshlrev_b64 v[178:179], 11, v[176:177]
	v_ashrrev_i32_e32 v173, 31, v172
	v_or_b32_e32 v168, 48, v164
	global_load_dwordx4 v[180:183], v[130:131], off
	global_load_dwordx4 v[154:157], v[130:131], off offset:256
	v_lshl_add_u64 v[130:131], v[166:167], 0, v[178:179]
	v_lshlrev_b64 v[174:175], 11, v[172:173]
	v_ashrrev_i32_e32 v169, 31, v168
	global_load_dwordx4 v[150:153], v[130:131], off
	global_load_dwordx4 v[146:149], v[130:131], off offset:256
	v_lshl_add_u64 v[130:131], v[166:167], 0, v[174:175]
	v_lshlrev_b64 v[170:171], 11, v[168:169]
	global_load_dwordx4 v[142:145], v[130:131], off
	global_load_dwordx4 v[138:141], v[130:131], off offset:256
	v_lshl_add_u64 v[130:131], v[166:167], 0, v[170:171]
	global_load_dwordx4 v[134:137], v[130:131], off
	s_nop 0
	global_load_dwordx4 v[130:133], v[130:131], off offset:256
	s_mov_b64 s[100:101], 0x40000
	v_lshl_add_u64 v[216:217], v[166:167], 0, v[186:187]
	v_lshl_add_u64 v[216:217], v[216:217], 0, s[100:101]
	global_load_dwordx4 v[230:233], v[216:217], off
	global_load_dwordx4 v[234:237], v[216:217], off offset:256
	v_lshl_add_u64 v[216:217], v[166:167], 0, v[178:179]
	v_lshl_add_u64 v[216:217], v[216:217], 0, s[100:101]
	global_load_dwordx4 v[238:241], v[216:217], off
	global_load_dwordx4 v[242:245], v[216:217], off offset:256
	v_lshl_add_u64 v[216:217], v[166:167], 0, v[174:175]
	v_lshl_add_u64 v[216:217], v[216:217], 0, s[100:101]
	global_load_dwordx4 v[246:249], v[216:217], off
	global_load_dwordx4 v[250:253], v[216:217], off offset:256
	v_lshl_add_u64 v[216:217], v[166:167], 0, v[170:171]
	v_lshl_add_u64 v[216:217], v[216:217], 0, s[100:101]
	global_load_dwordx4 v[222:225], v[216:217], off
	global_load_dwordx4 v[212:215], v[216:217], off offset:256
	v_lshl_add_u64 v[186:187], s[12:13], 0, v[186:187]
	v_lshl_add_u64 v[184:185], v[186:187], 0, v[184:185]
	s_and_b64 vcc, exec, s[16:17]
	s_mov_b32 s71, 0x1c000
	v_readlane_b32 s80, v255, 1
	s_mov_b64 s[76:77], 0x100
	s_waitcnt vmcnt(8)
	v_lshlrev_b32_e32 v186, 16, v180
	v_and_b32_e32 v187, 0xffff0000, v180
	v_lshlrev_b32_e32 v180, 16, v181
	v_and_b32_e32 v181, 0xffff0000, v181
	v_lshlrev_b32_e32 v192, 16, v182
	v_and_b32_e32 v193, 0xffff0000, v182
	v_lshlrev_b32_e32 v194, 16, v183
	v_and_b32_e32 v195, 0xffff0000, v183
	v_pk_add_f32 v[180:181], v[128:129], v[180:181]
	v_pk_add_f32 v[182:183], v[126:127], v[186:187]
	v_pk_add_f32 v[126:127], v[124:125], v[194:195]
	v_pk_add_f32 v[128:129], v[122:123], v[192:193]
	v_cvt_pk_bf16_f32 v122, v182, v183
	v_cvt_pk_bf16_f32 v123, v180, v181
	s_nop 0
	v_cvt_pk_bf16_f32 v124, v128, v129
	v_cvt_pk_bf16_f32 v125, v126, v127
	s_cbranch_vccz .LBB0_1391
	global_store_dwordx4 v[184:185], v[122:125], off
	s_cbranch_execnz .LBB0_1308

; __device__ __forceinline__ unsigned cvt_pk_bf16(float lo, float hi) { unsigned r; asm volatile("v_cvt_pk_bf16_f32 %0, %1, %2" : "=v"(r) : "v"(lo), "v"(hi)); return r; }
; __device__ __forceinline__ void st_wt16(void* p, u32x4 v) { asm volatile("global_store_dwordx4 %0, %1, off sc1\n\ts_nop 1" :: "v"(p), "v"(v) : "memory"); }
;     __device__ __forceinline__ void operator()(const f32x4 (&acc)[2][2][4][2], const Unit& u, int wr, int wc, int fr, int fq) const {
;     ...
;         for (int ai = 0; ai < 2; ++ai) {
;             u32x4 bb[4][2]; f32x4 bf0[4][2], bf1[4][2];
; #pragma unroll
;             for (int m = 0; m < 4; ++m)
; #pragma unroll
;                 for (int bj = 0; bj < 2; ++bj) { const size_t off = (size_t)(row0 + ai * HALF + m * 16) * D + col0 + bj * HALF;
;                     if constexpr (BASE_F32) { bf0[m][bj] = *(const f32x4*)(basef + off); bf1[m][bj] = *(const f32x4*)(basef + off + 4); } else bb[m][bj] = *(const u32x4*)(hb + off); }
;             u32x2 p8[4][2];
; #pragma unroll
;             for (int m = 0; m < 4; ++m) {
;                 const int row = row0 + ai * HALF + m * 16; const size_t off = (size_t)row * D + col0; float ss = 0.f;
; #pragma unroll
;                 for (int bj = 0; bj < 2; ++bj) {
;                     f32x4 h0, h1;
;                     if constexpr (BASE_F32) { h0 = bf0[m][bj]; h1 = bf1[m][bj]; }
;                     else { const u32x4 b = bb[m][bj];
;                         h0 = (f32x4){__uint_as_float(b.x << 16), __uint_as_float(b.x & 0xffff0000u), __uint_as_float(b.y << 16), __uint_as_float(b.y & 0xffff0000u)};
;                         h1 = (f32x4){__uint_as_float(b.z << 16), __uint_as_float(b.z & 0xffff0000u), __uint_as_float(b.w << 16), __uint_as_float(b.w & 0xffff0000u)}; }
;                     h0 = h0 + acc[ai][bj][m][0]; h1 = h1 + acc[ai][bj][m][1];
;                     u32x4 w; w.x = cvt_pk_bf16(h0[0], h0[1]); w.y = cvt_pk_bf16(h0[2], h0[3]); w.z = cvt_pk_bf16(h1[0], h1[1]); w.w = cvt_pk_bf16(h1[2], h1[3]);
;                     if (WT && wt) st_wt16(hb + HO + off + bj * HALF, w); else *(u32x4*)(hb + HO + off + bj * HALF) = w;
.LBB0_1345:
	s_or_b64 exec, exec, s[30:31]
	v_add_u32_e32 v106, 0x80, v164
	v_ashrrev_i32_e32 v107, 31, v106
	v_add_u32_e32 v102, 0x90, v164
	v_lshlrev_b64 v[112:113], 11, v[106:107]
	v_ashrrev_i32_e32 v103, 31, v102
	v_add_u32_e32 v98, 0xa0, v164
	v_lshl_add_u64 v[66:67], v[166:167], 0, v[112:113]
	v_lshlrev_b64 v[104:105], 11, v[102:103]
	v_ashrrev_i32_e32 v99, 31, v98
	v_add_u32_e32 v94, 0xb0, v164
	s_waitcnt vmcnt(8)
	v_mov_b64_e32 v[108:109], v[230:231]
	v_mov_b64_e32 v[110:111], v[232:233]
	v_mov_b64_e32 v[90:91], v[234:235]
	v_mov_b64_e32 v[92:93], v[236:237]
	v_lshl_add_u64 v[66:67], v[166:167], 0, v[104:105]
	v_lshlrev_b64 v[100:101], 11, v[98:99]
	v_ashrrev_i32_e32 v95, 31, v94
	v_mov_b64_e32 v[86:87], v[238:239]
	v_mov_b64_e32 v[88:89], v[240:241]
	v_mov_b64_e32 v[82:83], v[242:243]
	v_mov_b64_e32 v[84:85], v[244:245]
	v_lshl_add_u64 v[66:67], v[166:167], 0, v[100:101]
	v_lshlrev_b64 v[96:97], 11, v[94:95]
	v_mov_b64_e32 v[78:79], v[246:247]
	v_mov_b64_e32 v[80:81], v[248:249]
	v_mov_b64_e32 v[74:75], v[250:251]
	v_mov_b64_e32 v[76:77], v[252:253]
	v_lshl_add_u64 v[66:67], v[166:167], 0, v[96:97]
	v_mov_b64_e32 v[70:71], v[222:223]
	v_mov_b64_e32 v[72:73], v[224:225]
	s_nop 0
	v_mov_b64_e32 v[66:67], v[212:213]
	v_mov_b64_e32 v[68:69], v[214:215]
	v_lshl_add_u64 v[112:113], s[12:13], 0, v[112:113]
	s_and_b64 vcc, exec, s[4:5]
	v_lshl_add_u64 v[112:113], v[162:163], 1, v[112:113]
	v_lshlrev_b32_e32 v114, 16, v108
	v_and_b32_e32 v115, 0xffff0000, v108
	v_lshlrev_b32_e32 v108, 16, v109
	v_and_b32_e32 v109, 0xffff0000, v109
	v_lshlrev_b32_e32 v116, 16, v110
	v_and_b32_e32 v117, 0xffff0000, v110
	v_lshlrev_b32_e32 v118, 16, v111
	v_and_b32_e32 v119, 0xffff0000, v111
	v_pk_add_f32 v[108:109], v[62:63], v[108:109]
	v_pk_add_f32 v[110:111], v[60:61], v[114:115]
	v_pk_add_f32 v[60:61], v[58:59], v[118:119]
	v_pk_add_f32 v[62:63], v[56:57], v[116:117]
	v_cvt_pk_bf16_f32 v56, v110, v111
	v_cvt_pk_bf16_f32 v57, v108, v109
	s_nop 0
	v_cvt_pk_bf16_f32 v58, v62, v63
	v_cvt_pk_bf16_f32 v59, v60, v61
	s_cbranch_vccnz .LBB0_1399
	global_store_dwordx4 v[112:113], v[56:59], off
	s_cbranch_execnz .LBB0_1348
